# v55 + layer-0 norm phases: a token's eight row pieces fetched in one round trip (was 3 and 2)
# speedup vs baseline: 1.0126x; 1.0043x over previous
.LBB6_2026:
	v_lshl_add_u64 v[36:37], s[38:39], 0, v[68:69]
	v_add_co_u32_e32 v38, vcc, 0x200000, v36
	v_add_u32_e32 v64, s6, v64
	s_nop 0
	v_addc_co_u32_e32 v39, vcc, 0, v37, vcc
	global_load_dwordx4 v[78:81], v[38:39], off
	global_load_dwordx4 v[56:59], v[38:39], off offset:1024
	global_load_dwordx4 v[48:51], v[38:39], off offset:2048
	global_load_dwordx4 v[44:47], v[38:39], off offset:3072
	v_add_co_u32_e32 v86, vcc, 0x1000, v38
	s_nop 1
	v_addc_co_u32_e32 v87, vcc, 0, v39, vcc
	global_load_dwordx4 v[88:91], v[86:87], off
	global_load_dwordx4 v[92:95], v[86:87], off offset:1024
	global_load_dwordx4 v[96:99], v[86:87], off offset:2048
	global_load_dwordx4 v[100:103], v[86:87], off offset:3072
	v_lshl_add_u64 v[68:69], v[68:69], 0, s[10:11]
	s_waitcnt vmcnt(0)
	v_mul_f32_e32 v2, v79, v79
	v_mul_f32_e32 v40, v57, v57
	v_fmac_f32_e32 v2, v78, v78
	v_fmac_f32_e32 v40, v56, v56
	v_fmac_f32_e32 v2, v80, v80
	v_fmac_f32_e32 v40, v58, v58
	v_fmac_f32_e32 v2, v81, v81
	v_fmac_f32_e32 v40, v59, v59
	v_add_f32_e32 v2, v2, v40
	v_mul_f32_e32 v40, v49, v49
	v_fmac_f32_e32 v40, v48, v48
	v_fmac_f32_e32 v40, v50, v50
	v_mul_f32_e32 v38, v45, v45
	v_fmac_f32_e32 v40, v51, v51
	v_fmac_f32_e32 v38, v44, v44
	v_add_f32_e32 v2, v2, v40
	v_fmac_f32_e32 v38, v46, v46
	v_add_co_u32_e32 v40, vcc, s8, v36
	v_fmac_f32_e32 v38, v47, v47
	s_nop 0
	v_addc_co_u32_e32 v41, vcc, 0, v37, vcc
	v_add_f32_e32 v2, v2, v38
	v_mov_b64_e32 v[52:53], v[88:89]
	v_mov_b64_e32 v[54:55], v[90:91]
	v_mov_b64_e32 v[36:37], v[92:93]
	v_mov_b64_e32 v[38:39], v[94:95]
	v_mov_b32_e32 v60, v53
	v_mov_b32_e32 v61, v37
	v_mov_b32_e32 v42, v52
	v_mov_b32_e32 v43, v36
	v_pk_mul_f32 v[60:61], v[60:61], v[60:61]
	s_nop 0
	v_pk_fma_f32 v[42:43], v[42:43], v[42:43], v[60:61]
	v_mov_b32_e32 v60, v54
	v_mov_b32_e32 v61, v38
	v_pk_fma_f32 v[42:43], v[60:61], v[60:61], v[42:43]
	v_mov_b32_e32 v60, v55
	v_mov_b32_e32 v61, v39
	v_pk_fma_f32 v[42:43], v[60:61], v[60:61], v[42:43]
	s_nop 0
	v_add_f32_e32 v2, v2, v42
	v_add_f32_e32 v2, v2, v43
	v_mov_b64_e32 v[60:61], v[96:97]
	v_mov_b64_e32 v[62:63], v[98:99]
	s_nop 0
	v_mov_b64_e32 v[40:41], v[100:101]
	v_mov_b64_e32 v[42:43], v[102:103]
	v_mov_b32_e32 v82, v61
	v_mov_b32_e32 v83, v41
	v_mov_b32_e32 v70, v60
	v_mov_b32_e32 v71, v40
	v_pk_mul_f32 v[82:83], v[82:83], v[82:83]
	s_nop 0
	v_pk_fma_f32 v[70:71], v[70:71], v[70:71], v[82:83]
	v_mov_b32_e32 v82, v62
	v_mov_b32_e32 v83, v42
	v_pk_fma_f32 v[70:71], v[82:83], v[82:83], v[70:71]
	v_mov_b32_e32 v82, v63
	v_mov_b32_e32 v83, v43
	v_pk_fma_f32 v[70:71], v[82:83], v[82:83], v[70:71]
	s_nop 0
	v_add_f32_e32 v2, v2, v70
	v_add_f32_e32 v2, v2, v71
	ds_bpermute_b32 v65, v72, v2
	s_waitcnt lgkmcnt(0)
	v_add_f32_e32 v2, v2, v65
	ds_bpermute_b32 v65, v73, v2
	s_waitcnt lgkmcnt(0)
	v_add_f32_e32 v2, v2, v65
	ds_bpermute_b32 v65, v74, v2
	s_waitcnt lgkmcnt(0)
	v_add_f32_e32 v2, v2, v65
	ds_bpermute_b32 v65, v75, v2
	s_waitcnt lgkmcnt(0)
	v_add_f32_e32 v2, v2, v65
	ds_bpermute_b32 v65, v76, v2
	s_waitcnt lgkmcnt(0)
	v_add_f32_e32 v2, v2, v65
	ds_bpermute_b32 v65, v77, v2
	s_waitcnt lgkmcnt(0)
	v_add_f32_e32 v2, v2, v65
	v_fmamk_f32 v2, v2, 0x3a000000, v212
	v_cmp_gt_f32_e32 vcc, s58, v2
	v_mul_f32_e32 v65, 0x4b800000, v2
	s_nop 0
	v_cndmask_b32_e32 v2, v2, v65, vcc
	v_rsq_f32_e32 v2, v2
	s_nop 0
	v_mul_f32_e32 v65, 0x45800000, v2
	v_cndmask_b32_e32 v2, v2, v65, vcc
	v_pk_mul_f32 v[70:71], v[78:79], v[2:3] op_sel_hi:[1,0]
	v_pk_mul_f32 v[78:79], v[80:81], v[2:3] op_sel_hi:[1,0]
	v_pk_mul_f32 v[70:71], v[4:5], v[70:71]
	v_pk_mul_f32 v[78:79], v[6:7], v[78:79]
	v_cvt_pk_bf16_f32 v70, v70, v71
	v_cvt_pk_bf16_f32 v71, v78, v79
	v_lshl_add_u64 v[78:79], s[38:39], 0, v[66:67]
	v_pk_mul_f32 v[36:37], v[36:37], v[2:3] op_sel_hi:[1,0]
	v_pk_mul_f32 v[38:39], v[38:39], v[2:3] op_sel_hi:[1,0]
	v_add_co_u32_e32 v78, vcc, s9, v78
	v_pk_mul_f32 v[36:37], v[24:25], v[36:37]
	v_pk_mul_f32 v[38:39], v[26:27], v[38:39]
	v_addc_co_u32_e32 v79, vcc, 0, v79, vcc
	v_cvt_pk_bf16_f32 v36, v36, v37
	v_cvt_pk_bf16_f32 v37, v38, v39
	v_pk_mul_f32 v[44:45], v[44:45], v[2:3] op_sel_hi:[1,0]
	v_pk_mul_f32 v[46:47], v[46:47], v[2:3] op_sel_hi:[1,0]
	global_store_dwordx2 v[78:79], v[36:37], off offset:2560
	v_pk_mul_f32 v[36:37], v[60:61], v[2:3] op_sel_hi:[1,0]
	v_pk_mul_f32 v[38:39], v[62:63], v[2:3] op_sel_hi:[1,0]
	v_pk_mul_f32 v[44:45], v[16:17], v[44:45]
	v_pk_mul_f32 v[46:47], v[18:19], v[46:47]
	v_pk_mul_f32 v[36:37], v[28:29], v[36:37]
	v_pk_mul_f32 v[38:39], v[30:31], v[38:39]
	v_cvt_pk_bf16_f32 v44, v44, v45
	v_cvt_pk_bf16_f32 v45, v46, v47
	v_cvt_pk_bf16_f32 v36, v36, v37
	v_cvt_pk_bf16_f32 v37, v38, v39
	v_pk_mul_f32 v[56:57], v[56:57], v[2:3] op_sel_hi:[1,0]
	v_pk_mul_f32 v[58:59], v[58:59], v[2:3] op_sel_hi:[1,0]
	v_pk_mul_f32 v[48:49], v[48:49], v[2:3] op_sel_hi:[1,0]
	v_pk_mul_f32 v[50:51], v[50:51], v[2:3] op_sel_hi:[1,0]
	global_store_dwordx2 v[78:79], v[44:45], off offset:1536
	v_pk_mul_f32 v[44:45], v[52:53], v[2:3] op_sel_hi:[1,0]
	v_pk_mul_f32 v[46:47], v[54:55], v[2:3] op_sel_hi:[1,0]
	global_store_dwordx2 v[78:79], v[36:37], off offset:3072
	v_pk_mul_f32 v[36:37], v[40:41], v[2:3] op_sel_hi:[1,0]
	v_pk_mul_f32 v[38:39], v[42:43], v[2:3] op_sel_hi:[1,0]
	v_pk_mul_f32 v[56:57], v[8:9], v[56:57]
	v_pk_mul_f32 v[58:59], v[10:11], v[58:59]
	v_pk_mul_f32 v[48:49], v[12:13], v[48:49]
	v_pk_mul_f32 v[50:51], v[14:15], v[50:51]
	v_pk_mul_f32 v[44:45], v[20:21], v[44:45]
	v_pk_mul_f32 v[46:47], v[22:23], v[46:47]
	v_pk_mul_f32 v[36:37], v[32:33], v[36:37]
	v_pk_mul_f32 v[38:39], v[34:35], v[38:39]
	v_cmp_lt_i32_e32 vcc, s7, v64
	v_cvt_pk_bf16_f32 v56, v56, v57
	v_cvt_pk_bf16_f32 v57, v58, v59
	v_cvt_pk_bf16_f32 v48, v48, v49
	v_cvt_pk_bf16_f32 v49, v50, v51
	v_cvt_pk_bf16_f32 v44, v44, v45
	v_cvt_pk_bf16_f32 v45, v46, v47
	v_cvt_pk_bf16_f32 v36, v36, v37
	v_cvt_pk_bf16_f32 v37, v38, v39
	v_lshl_add_u64 v[66:67], v[66:67], 0, s[12:13]
	s_or_b64 s[4:5], vcc, s[4:5]
	global_store_dwordx2 v[78:79], v[70:71], off
	global_store_dwordx2 v[78:79], v[56:57], off offset:512
	global_store_dwordx2 v[78:79], v[48:49], off offset:1024
	global_store_dwordx2 v[78:79], v[44:45], off offset:2048
	global_store_dwordx2 v[78:79], v[36:37], off offset:3584
	s_andn2_b64 exec, exec, s[4:5]
	s_cbranch_execnz .LBB6_2026

.LBB6_2212:
	v_lshl_add_u64 v[36:37], s[38:39], 0, v[70:71]
	v_add_co_u32_e32 v38, vcc, 0x200000, v36
	s_mov_b32 s0, 0x20c00000
	s_nop 0
	v_addc_co_u32_e32 v39, vcc, 0, v37, vcc
	global_load_dwordx4 v[72:75], v[38:39], off
	global_load_dwordx4 v[60:63], v[38:39], off offset:1024
	global_load_dwordx4 v[56:59], v[38:39], off offset:2048
	global_load_dwordx4 v[52:55], v[38:39], off offset:3072
	v_add_co_u32_e32 v36, vcc, s8, v36
	v_add_u32_e32 v64, s6, v64
	s_nop 0
	v_addc_co_u32_e32 v37, vcc, 0, v37, vcc
	global_load_dwordx4 v[48:51], v[36:37], off
	global_load_dwordx4 v[44:47], v[36:37], off offset:1024
	global_load_dwordx4 v[88:91], v[36:37], off offset:2048
	global_load_dwordx4 v[92:95], v[36:37], off offset:3072
	v_lshl_add_u64 v[70:71], v[70:71], 0, s[10:11]
	s_waitcnt vmcnt(0)
	v_mul_f32_e32 v2, v73, v73
	v_mul_f32_e32 v40, v61, v61
	v_fmac_f32_e32 v2, v72, v72
	v_fmac_f32_e32 v40, v60, v60
	v_fmac_f32_e32 v2, v74, v74
	v_fmac_f32_e32 v40, v62, v62
	v_fmac_f32_e32 v2, v75, v75
	v_fmac_f32_e32 v40, v63, v63
	v_add_f32_e32 v2, v2, v40
	v_mul_f32_e32 v40, v57, v57
	v_fmac_f32_e32 v40, v56, v56
	v_mul_f32_e32 v38, v53, v53
	v_fmac_f32_e32 v40, v58, v58
	v_fmac_f32_e32 v38, v52, v52
	v_fmac_f32_e32 v40, v59, v59
	v_fmac_f32_e32 v38, v54, v54
	v_add_f32_e32 v2, v2, v40
	v_fmac_f32_e32 v38, v55, v55
	v_mov_b32_e32 v40, v49
	v_mov_b32_e32 v41, v45
	v_add_f32_e32 v2, v2, v38
	v_mov_b32_e32 v38, v48
	v_mov_b32_e32 v39, v44
	v_pk_mul_f32 v[40:41], v[40:41], v[40:41]
	s_nop 0
	v_pk_fma_f32 v[38:39], v[38:39], v[38:39], v[40:41]
	v_mov_b32_e32 v40, v50
	v_mov_b32_e32 v41, v46
	v_pk_fma_f32 v[38:39], v[40:41], v[40:41], v[38:39]
	v_mov_b32_e32 v40, v51
	v_mov_b32_e32 v41, v47
	v_pk_fma_f32 v[38:39], v[40:41], v[40:41], v[38:39]
	s_nop 0
	v_add_f32_e32 v2, v2, v38
	v_add_f32_e32 v2, v2, v39
	v_mov_b64_e32 v[40:41], v[88:89]
	v_mov_b64_e32 v[42:43], v[90:91]
	s_nop 0
	v_mov_b64_e32 v[36:37], v[92:93]
	v_mov_b64_e32 v[38:39], v[94:95]
	v_mov_b32_e32 v78, v41
	v_mov_b32_e32 v79, v37
	v_mov_b32_e32 v76, v40
	v_mov_b32_e32 v77, v36
	v_pk_mul_f32 v[78:79], v[78:79], v[78:79]
	s_nop 0
	v_pk_fma_f32 v[76:77], v[76:77], v[76:77], v[78:79]
	v_mov_b32_e32 v78, v42
	v_mov_b32_e32 v79, v38
	v_pk_fma_f32 v[76:77], v[78:79], v[78:79], v[76:77]
	v_mov_b32_e32 v78, v43
	v_mov_b32_e32 v79, v39
	v_pk_fma_f32 v[76:77], v[78:79], v[78:79], v[76:77]
	s_nop 0
	v_add_f32_e32 v2, v2, v76
	v_add_f32_e32 v2, v2, v77
	ds_bpermute_b32 v65, v80, v2
	s_waitcnt lgkmcnt(0)
	v_add_f32_e32 v2, v2, v65
	ds_bpermute_b32 v65, v81, v2
	s_waitcnt lgkmcnt(0)
	v_add_f32_e32 v2, v2, v65
	ds_bpermute_b32 v65, v82, v2
	s_waitcnt lgkmcnt(0)
	v_add_f32_e32 v2, v2, v65
	ds_bpermute_b32 v65, v83, v2
	s_waitcnt lgkmcnt(0)
	v_add_f32_e32 v2, v2, v65
	ds_bpermute_b32 v65, v84, v2
	s_waitcnt lgkmcnt(0)
	v_add_f32_e32 v2, v2, v65
	ds_bpermute_b32 v65, v85, v2
	s_waitcnt lgkmcnt(0)
	v_add_f32_e32 v2, v2, v65
	v_fmamk_f32 v2, v2, 0x3a000000, v212
	v_cmp_gt_f32_e32 vcc, s58, v2
	v_mul_f32_e32 v65, 0x4b800000, v2
	s_nop 0
	v_cndmask_b32_e32 v2, v2, v65, vcc
	v_rsq_f32_e32 v2, v2
	s_nop 0
	v_mul_f32_e32 v65, 0x45800000, v2
	v_cndmask_b32_e32 v2, v2, v65, vcc
	v_pk_mul_f32 v[72:73], v[72:73], v[2:3] op_sel_hi:[1,0]
	v_pk_mul_f32 v[74:75], v[74:75], v[2:3] op_sel_hi:[1,0]
	v_pk_mul_f32 v[72:73], v[4:5], v[72:73]
	v_pk_mul_f32 v[76:77], v[6:7], v[74:75]
	v_cvt_pk_bf16_f32 v78, v72, v73
	v_cvt_pk_bf16_f32 v79, v76, v77
	v_mul_f32_e32 v65, 4.0, v77
	v_mul_f32_e32 v73, 4.0, v73
	v_mul_f32_e32 v72, 4.0, v72
	v_mov_b32_e32 v77, v3
	v_cvt_pk_fp8_f32 v77, v72, v73
	v_pk_mul_f32 v[60:61], v[60:61], v[2:3] op_sel_hi:[1,0]
	v_lshl_add_u64 v[74:75], s[38:39], 0, v[68:69]
	v_mul_f32_e32 v76, 4.0, v76
	v_pk_mul_f32 v[60:61], v[8:9], v[60:61]
	v_pk_mul_f32 v[56:57], v[56:57], v[2:3] op_sel_hi:[1,0]
	v_pk_mul_f32 v[58:59], v[58:59], v[2:3] op_sel_hi:[1,0]
	v_add_co_u32_e32 v74, vcc, s9, v74
	v_cvt_pk_fp8_f32 v77, v76, v65 op_sel:[0,0,1]
	v_cvt_pk_bf16_f32 v76, v60, v61
	v_mul_f32_e32 v61, 4.0, v61
	v_mul_f32_e32 v60, 4.0, v60
	v_mov_b32_e32 v65, v3
	v_pk_mul_f32 v[56:57], v[12:13], v[56:57]
	v_pk_mul_f32 v[58:59], v[14:15], v[58:59]
	v_addc_co_u32_e32 v75, vcc, 0, v75, vcc
	v_cvt_pk_fp8_f32 v65, v60, v61
	v_cvt_pk_bf16_f32 v60, v56, v57
	v_cvt_pk_bf16_f32 v61, v58, v59
	v_pk_mul_f32 v[52:53], v[52:53], v[2:3] op_sel_hi:[1,0]
	v_pk_mul_f32 v[54:55], v[54:55], v[2:3] op_sel_hi:[1,0]
	global_store_dwordx2 v[74:75], v[60:61], off offset:1024
	v_mul_f32_e32 v57, 4.0, v57
	v_mul_f32_e32 v56, 4.0, v56
	v_mov_b32_e32 v60, v3
	v_pk_mul_f32 v[52:53], v[16:17], v[52:53]
	v_pk_mul_f32 v[54:55], v[18:19], v[54:55]
	v_cvt_pk_fp8_f32 v60, v56, v57
	v_cvt_pk_bf16_f32 v56, v52, v53
	v_cvt_pk_bf16_f32 v57, v54, v55
	v_pk_mul_f32 v[48:49], v[48:49], v[2:3] op_sel_hi:[1,0]
	v_pk_mul_f32 v[50:51], v[50:51], v[2:3] op_sel_hi:[1,0]
	global_store_dwordx2 v[74:75], v[56:57], off offset:1536
	v_mul_f32_e32 v53, 4.0, v53
	v_mul_f32_e32 v52, 4.0, v52
	v_mov_b32_e32 v56, v3
	v_pk_mul_f32 v[48:49], v[20:21], v[48:49]
	v_pk_mul_f32 v[50:51], v[22:23], v[50:51]
	v_cvt_pk_fp8_f32 v56, v52, v53
	v_cvt_pk_bf16_f32 v52, v48, v49
	v_cvt_pk_bf16_f32 v53, v50, v51
	v_pk_mul_f32 v[44:45], v[44:45], v[2:3] op_sel_hi:[1,0]
	v_pk_mul_f32 v[46:47], v[46:47], v[2:3] op_sel_hi:[1,0]
	global_store_dwordx2 v[74:75], v[52:53], off offset:2048
	v_mul_f32_e32 v49, 4.0, v49
	v_mul_f32_e32 v48, 4.0, v48
	v_mov_b32_e32 v52, v3
	v_pk_mul_f32 v[44:45], v[24:25], v[44:45]
	v_pk_mul_f32 v[46:47], v[26:27], v[46:47]
	v_cvt_pk_fp8_f32 v52, v48, v49
	v_cvt_pk_bf16_f32 v48, v44, v45
	v_cvt_pk_bf16_f32 v49, v46, v47
	v_pk_mul_f32 v[40:41], v[40:41], v[2:3] op_sel_hi:[1,0]
	v_pk_mul_f32 v[42:43], v[42:43], v[2:3] op_sel_hi:[1,0]
	global_store_dwordx2 v[74:75], v[48:49], off offset:2560
	v_mul_f32_e32 v45, 4.0, v45
	v_mul_f32_e32 v44, 4.0, v44
	v_mov_b32_e32 v48, v3
	v_pk_mul_f32 v[40:41], v[28:29], v[40:41]
	v_pk_mul_f32 v[42:43], v[30:31], v[42:43]
	v_cvt_pk_fp8_f32 v48, v44, v45
	v_cvt_pk_bf16_f32 v44, v40, v41
	v_cvt_pk_bf16_f32 v45, v42, v43
	v_pk_mul_f32 v[36:37], v[36:37], v[2:3] op_sel_hi:[1,0]
	v_pk_mul_f32 v[38:39], v[38:39], v[2:3] op_sel_hi:[1,0]
	global_store_dwordx2 v[74:75], v[44:45], off offset:3072
	v_mul_f32_e32 v41, 4.0, v41
	v_mul_f32_e32 v40, 4.0, v40
	v_mov_b32_e32 v44, v3
	v_pk_mul_f32 v[36:37], v[32:33], v[36:37]
	v_pk_mul_f32 v[38:39], v[34:35], v[38:39]
	v_pk_mul_f32 v[62:63], v[62:63], v[2:3] op_sel_hi:[1,0]
	v_cvt_pk_fp8_f32 v44, v40, v41
	v_cvt_pk_bf16_f32 v40, v36, v37
	v_cvt_pk_bf16_f32 v41, v38, v39
	v_mul_f32_e32 v2, 4.0, v39
	v_mul_f32_e32 v37, 4.0, v37
	v_mul_f32_e32 v36, 4.0, v36
	v_mov_b32_e32 v39, v3
	global_store_dwordx2 v[74:75], v[78:79], off
	v_lshl_add_u64 v[78:79], s[38:39], 0, v[66:67]
	v_cvt_pk_fp8_f32 v39, v36, v37
	v_add_co_u32_e32 v72, vcc, s0, v78
	v_pk_mul_f32 v[62:63], v[10:11], v[62:63]
	s_nop 0
	v_addc_co_u32_e32 v73, vcc, 0, v79, vcc
	global_store_dword v[72:73], v77, off
	v_cvt_pk_bf16_f32 v77, v62, v63
	v_mul_f32_e32 v63, 4.0, v63
	v_mul_f32_e32 v62, 4.0, v62
	v_mul_f32_e32 v59, 4.0, v59
	v_mul_f32_e32 v58, 4.0, v58
	v_mul_f32_e32 v55, 4.0, v55
	v_mul_f32_e32 v54, 4.0, v54
	v_mul_f32_e32 v51, 4.0, v51
	v_mul_f32_e32 v50, 4.0, v50
	v_mul_f32_e32 v47, 4.0, v47
	v_mul_f32_e32 v46, 4.0, v46
	v_mul_f32_e32 v43, 4.0, v43
	v_mul_f32_e32 v42, 4.0, v42
	v_mul_f32_e32 v38, 4.0, v38
	v_cvt_pk_fp8_f32 v65, v62, v63 op_sel:[0,0,1]
	v_cvt_pk_fp8_f32 v60, v58, v59 op_sel:[0,0,1]
	v_cvt_pk_fp8_f32 v56, v54, v55 op_sel:[0,0,1]
	v_cvt_pk_fp8_f32 v52, v50, v51 op_sel:[0,0,1]
	v_cvt_pk_fp8_f32 v48, v46, v47 op_sel:[0,0,1]
	v_cvt_pk_fp8_f32 v44, v42, v43 op_sel:[0,0,1]
	v_cvt_pk_fp8_f32 v39, v38, v2 op_sel:[0,0,1]
	v_cmp_lt_i32_e32 vcc, s7, v64
	v_lshl_add_u64 v[66:67], v[66:67], 0, s[14:15]
	v_lshl_add_u64 v[68:69], v[68:69], 0, s[12:13]
	s_or_b64 s[4:5], vcc, s[4:5]
	global_store_dwordx2 v[74:75], v[76:77], off offset:512
	global_store_dword v[72:73], v65, off offset:256
	global_store_dword v[72:73], v60, off offset:512
	global_store_dword v[72:73], v56, off offset:768
	global_store_dword v[72:73], v52, off offset:1024
	global_store_dword v[72:73], v48, off offset:1280
	global_store_dword v[72:73], v44, off offset:1536
	global_store_dwordx2 v[74:75], v[40:41], off offset:3584
	global_store_dword v[72:73], v39, off offset:1792
	s_andn2_b64 exec, exec, s[4:5]
	s_cbranch_execnz .LBB6_2212
